# strategy 4, other half: static s_setprio 1 for waves 0-3 during the attention units (timing only)
# speedup vs baseline: 1.0027x; 1.0027x over previous
.LBB0_400:
	s_mov_b64 s[8:9], -1
	s_and_b64 vcc, exec, s[6:7]
	s_cbranch_vccz .LBB0_393
	s_cmp_lt_u32 s67, 0x100
	s_cbranch_scc0 .Lap_skip
	s_setprio 1
